# scan pass 1: one static s_setprio 1 for waves 4-7 for the duration of the stage (reset before Fourier stage 0)
# speedup vs baseline: 1.0079x; 1.0079x over previous
.LBB0_346:
	s_or_b64 exec, exec, s[0:1]
	s_mov_b64 s[0:1], s[46:47]
	v_mov_b32_e32 v66, v186
	s_waitcnt lgkmcnt(0)
	s_barrier
	s_load_dwordx2 s[2:3], s[0:1], 0x98
	v_readlane_b32 s0, v235, 16
	s_cmpk_lt_i32 s0, 0x140
	v_readlane_b32 s1, v235, 17
	s_cbranch_scc0 .LBB0_368
	v_readfirstlane_b32 s99, v186
	s_nop 0
	s_lshr_b32 s99, s99, 6
	s_cmp_ge_u32 s99, 4
	s_cbranch_scc0 .Lscan_prio_done
	s_setprio 1
.Lscan_prio_done:
	s_waitcnt lgkmcnt(0)
	s_add_u32 s28, s2, 0x176f3000
	s_addc_u32 s29, s3, 0
	s_add_u32 s27, s2, 0xf1f3000
	v_and_b32_e32 v0, 63, v66
	s_addc_u32 s40, s3, 0
	s_add_u32 s30, s2, 0xd0f3000
	v_lshlrev_b32_e32 v40, 2, v0
	v_mov_b32_e32 v41, 0
	s_addc_u32 s31, s3, 0
	v_lshl_add_u64 v[0:1], s[2:3], 0, v[40:41]
	s_mov_b64 s[0:1], 0x152f3000
	s_add_u32 s34, s2, 0xc073000
	v_lshl_add_u64 v[42:43], v[0:1], 0, s[0:1]
	s_movk_i32 s41, 0x80
	v_readlane_b32 s0, v235, 16
	v_ashrrev_i32_e32 v67, 6, v66
	s_addc_u32 s35, s3, 0
	v_cmp_gt_i32_e64 s[8:9], s41, v66
	s_movk_i32 s42, 0x90
	s_mov_b32 s37, 0
	s_add_i32 s43, 0, 0x1d200
	s_mov_b32 s44, 0x1771b000
	s_add_i32 s45, 0, 0x18a00
	s_add_i32 s46, 0, 0x14200
	s_movk_i32 s47, 0x110
	s_mov_b32 s48, 0x5040100
	s_add_i32 s49, 0, 0x9800
	s_movk_i32 s50, 0x1000
	v_mov_b32_e32 v130, v41
	v_mov_b32_e32 v131, v41
	s_mov_b32 s51, s0
	v_readlane_b32 s1, v235, 17
	s_branch .LBB0_349

.LBB0_367:
	s_setprio 0
	v_readlane_b32 s46, v235, 14
	v_readlane_b32 s47, v235, 15
